# MLA loop: next-tile global loads issued inside the PV MFMA gaps
# speedup vs baseline: 1.0006x; 1.0006x over previous
; __device__ __forceinline__ void finishSM(f32x16& p0, f32x16& p1, float alpha, float& l_reg, bf16x8& pa0, bf16x8& pa1, bf16x8& pa2, bf16x8& pa3) {
; #pragma unroll
;     for (int r = 0; r < 16; ++r) p1[r] = EXP_PROBE ? fmaf(p1[r], 0.001f, 1.f) : __builtin_amdgcn_exp2f(p1[r]);
;     float ps = 0.f;
; #pragma unroll
;     for (int r = 0; r < 16; ++r) ps += p0[r];
; #pragma unroll
;     for (int r = 0; r < 16; ++r) ps += p1[r];
;     { auto rr = __builtin_amdgcn_permlane32_swap(__float_as_uint(ps), __float_as_uint(ps), false, false);
;       ps = __uint_as_float(rr[0]) + __uint_as_float(rr[1]); }
;     l_reg = l_reg * alpha + ps;
;     ATT_PKN(p0, 0, pa0); ATT_PKN(p0, 8, pa1); ATT_PKN(p1, 0, pa2); ATT_PKN(p1, 8, pa3);
; }
; template <int DQK> __device__ __forceinline__ void qkt(f32x16& p0, f32x16& p1, const LAS char* buf, const bf16x8* qr, int r32, int hi, const f32x16& negm) {
; #pragma unroll
;     for (int d0 = 0; d0 < 4; ++d0) { const int ch = d0 * 2 + hi;
;         const bf16x8 b0 = *(const LAS bf16x8*)(buf + B_KN + swz64(r32, ch));
;         const bf16x8 b1 = *(const LAS bf16x8*)(buf + B_KN + swz64(32 + r32, ch));
;         p0 = __builtin_amdgcn_mfma_f32_32x32x16_bf16(b0, qr[d0], d0 == 0 ? negm : p0, 0, 0, 0);
;         p1 = __builtin_amdgcn_mfma_f32_32x32x16_bf16(b1, qr[d0], d0 == 0 ? negm : p1, 0, 0, 0); }
;     if constexpr (DQK == 96) {
; #pragma unroll
;         for (int d0 = 0; d0 < 2; ++d0) { const int ch = d0 * 2 + hi;
;             const bf16x8 b0 = *(const LAS bf16x8*)(buf + B_KR + swz32(r32, ch));
;             const bf16x8 b1 = *(const LAS bf16x8*)(buf + B_KR + swz32(32 + r32, ch));
;             p0 = __builtin_amdgcn_mfma_f32_32x32x16_bf16(b0, qr[4 + d0], p0, 0, 0, 0);
;             p1 = __builtin_amdgcn_mfma_f32_32x32x16_bf16(b1, qr[4 + d0], p1, 0, 0, 0); }
;     }
; }
; template <int D0> __device__ __forceinline__ void pv_one(f32x16& od, unsigned vb, bf16x8 pa0, bf16x8 pa1, bf16x8 pa2, bf16x8 pa3) {
;     const s16x4 l0 = tr_read<v_rd_off(D0, 0, 0)>(vb), h0 = tr_read<v_rd_off(D0, 0, 1)>(vb), l1 = tr_read<v_rd_off(D0, 1, 0)>(vb), h1 = tr_read<v_rd_off(D0, 1, 1)>(vb);
;     const s16x4 l2 = tr_read<v_rd_off(D0, 2, 0)>(vb), h2 = tr_read<v_rd_off(D0, 2, 1)>(vb), l3 = tr_read<v_rd_off(D0, 3, 0)>(vb), h3 = tr_read<v_rd_off(D0, 3, 1)>(vb);
;     asm volatile("s_waitcnt lgkmcnt(0)" ::: "memory"); SBAR();
.LBB0_523:
	s_mov_b32 s10, s0
	s_waitcnt lgkmcnt(0)
	s_barrier
	v_add_u32_e32 v2, s13, v201
	v_add_u32_e32 v8, v2, v209
	ds_read_b128 v[4:7], v8
	ds_read_b128 v[8:11], v8 offset:4096
	v_add_u32_e32 v246, v2, v210
	ds_read_b128 v[174:177], v246
	ds_read_b128 v[246:249], v246 offset:4096
	v_add_u32_e32 v78, v2, v211
	ds_read_b128 v[250:253], v78
	ds_read_b128 v[78:81], v78 offset:4096
	v_add_u32_e32 v16, v2, v212
	ds_read_b128 v[12:15], v16
	v_add_u32_e32 v2, s13, v217
	v_exp_f32_e32 v98, v98
	v_exp_f32_e32 v99, v99
	v_exp_f32_e32 v100, v100
	v_exp_f32_e32 v101, v101
	v_exp_f32_e32 v102, v102
	v_exp_f32_e32 v103, v103
	v_exp_f32_e32 v104, v104
	v_exp_f32_e32 v105, v105
	s_waitcnt lgkmcnt(6)
	v_mfma_f32_32x32x16_bf16 v[130:145], v[4:7], v[166:169], v[82:97]
	ds_read_b128 v[4:7], v16 offset:4096
	v_exp_f32_e32 v106, v106
	v_exp_f32_e32 v107, v107
	v_exp_f32_e32 v108, v108
	v_cvt_pk_bf16_f32 v74, v243, v245
	s_waitcnt lgkmcnt(6)
	v_mfma_f32_32x32x16_bf16 v[114:129], v[8:11], v[166:169], v[82:97]
	v_add_u32_e32 v16, v2, v219
	ds_read_b128 v[8:11], v16 offset:8192
	v_exp_f32_e32 v109, v109
	v_exp_f32_e32 v110, v110
	v_exp_f32_e32 v111, v111
	v_cvt_pk_bf16_f32 v75, v241, v244
	s_waitcnt lgkmcnt(6)
	v_mfma_f32_32x32x16_bf16 v[130:145], v[174:177], v[162:165], v[130:145]
	ds_read_b128 v[174:177], v16 offset:10240
	v_exp_f32_e32 v112, v112
	v_exp_f32_e32 v113, v113
	v_cvt_pk_bf16_f32 v76, v239, v242
	v_cvt_pk_bf16_f32 v77, v238, v240
	v_add_f32_e32 v229, 0, v243
	v_add_f32_e32 v229, v245, v229
	s_waitcnt lgkmcnt(6)
	v_mfma_f32_32x32x16_bf16 v[114:129], v[246:249], v[162:165], v[114:129]
	v_add_u32_e32 v16, v2, v220
	ds_read_b128 v[246:249], v16 offset:8192
	v_cvt_pk_bf16_f32 v66, v236, v237
	v_cvt_pk_bf16_f32 v67, v233, v235
	v_add_f32_e32 v229, v241, v229
	v_add_f32_e32 v229, v244, v229
	v_add_f32_e32 v229, v239, v229
	v_add_f32_e32 v229, v242, v229
	s_waitcnt lgkmcnt(6)
	v_mfma_f32_32x32x16_bf16 v[130:145], v[250:253], v[158:161], v[130:145]
	ds_read_b128 v[250:253], v16 offset:10240
	v_cvt_pk_bf16_f32 v68, v231, v234
	v_cvt_pk_bf16_f32 v69, v230, v232
	v_add_f32_e32 v229, v238, v229
	v_add_f32_e32 v229, v240, v229
	v_add_f32_e32 v229, v236, v229
	v_add_f32_e32 v229, v237, v229
	s_waitcnt lgkmcnt(6)
	v_mfma_f32_32x32x16_bf16 v[114:129], v[78:81], v[158:161], v[114:129]
	v_add_f32_e32 v229, v233, v229
	v_add_f32_e32 v229, v235, v229
	v_add_f32_e32 v229, v231, v229
	v_add_f32_e32 v229, v234, v229
	v_add_f32_e32 v229, v230, v229
	v_add_f32_e32 v229, v232, v229
	s_waitcnt lgkmcnt(5)
	v_mfma_f32_32x32x16_bf16 v[130:145], v[12:15], v[154:157], v[130:145]
	v_add_u32_e32 v17, s11, v213
	ds_read_b64_tr_b16 v[230:231], v17 offset:0
	ds_read_b64_tr_b16 v[232:233], v17 offset:1024
	ds_read_b64_tr_b16 v[234:235], v17 offset:2048
	ds_read_b64_tr_b16 v[236:237], v17 offset:3072
	v_add_f32_e32 v229, v98, v229
	v_add_f32_e32 v229, v99, v229
	v_add_f32_e32 v229, v100, v229
	s_waitcnt lgkmcnt(8)
	v_mfma_f32_32x32x16_bf16 v[114:129], v[4:7], v[154:157], v[114:129]
	ds_read_b64_tr_b16 v[238:239], v17 offset:4096
	ds_read_b64_tr_b16 v[240:241], v17 offset:5120
	ds_read_b64_tr_b16 v[242:243], v17 offset:6144
	ds_read_b64_tr_b16 v[244:245], v17 offset:7168
	v_add_f32_e32 v229, v101, v229
	v_add_f32_e32 v229, v102, v229
	v_add_f32_e32 v229, v103, v229
	s_waitcnt lgkmcnt(11)
	v_mfma_f32_32x32x16_bf16 v[130:145], v[8:11], v[150:153], v[130:145]
	v_add_f32_e32 v229, v104, v229
	v_add_f32_e32 v229, v105, v229
	v_add_f32_e32 v229, v106, v229
	v_add_f32_e32 v229, v107, v229
	v_add_f32_e32 v229, v108, v229
	v_add_f32_e32 v229, v109, v229
	s_waitcnt lgkmcnt(10)
	v_mfma_f32_32x32x16_bf16 v[114:129], v[174:177], v[150:153], v[114:129]
	v_add_f32_e32 v229, v110, v229
	v_add_f32_e32 v229, v111, v229
	v_add_f32_e32 v229, v112, v229
	v_add_f32_e32 v228, v113, v229
	v_mov_b32_e32 v229, v228
	s_waitcnt lgkmcnt(9)
	v_mfma_f32_32x32x16_bf16 v[130:145], v[246:249], v[146:149], v[130:145]
	v_cvt_pk_bf16_f32 v70, v98, v99
	v_cvt_pk_bf16_f32 v71, v100, v101
	v_cvt_pk_bf16_f32 v72, v102, v103
	v_cvt_pk_bf16_f32 v73, v104, v105
	v_permlane32_swap_b32_e32 v228, v229
	s_waitcnt lgkmcnt(8)
	v_mfma_f32_32x32x16_bf16 v[114:129], v[250:253], v[146:149], v[114:129]
	v_cvt_pk_bf16_f32 v12, v106, v107
	v_cvt_pk_bf16_f32 v13, v108, v109
	v_cvt_pk_bf16_f32 v14, v110, v111
	v_cvt_pk_bf16_f32 v15, v112, v113
	ds_read_b64_tr_b16 v[78:79], v17 offset:512
	ds_read_b64_tr_b16 v[80:81], v17 offset:1536
	ds_read_b64_tr_b16 v[98:99], v17 offset:2560
	ds_read_b64_tr_b16 v[100:101], v17 offset:3584
	ds_read_b64_tr_b16 v[102:103], v17 offset:4608
	ds_read_b64_tr_b16 v[104:105], v17 offset:5632
	ds_read_b64_tr_b16 v[110:111], v17 offset:6656
	ds_read_b64_tr_b16 v[112:113], v17 offset:7680
	v_max3_f32 v2, v130, v131, v132
	v_max3_f32 v2, v2, v133, v134
	v_max3_f32 v2, v2, v135, v136
	v_max3_f32 v2, v2, v137, v138
	v_max3_f32 v2, v2, v139, v140
	v_max3_f32 v2, v2, v141, v142
	v_max3_f32 v2, v2, v143, v144
	v_max3_f32 v2, v2, v145, v114
	v_max3_f32 v2, v2, v115, v116
	s_waitcnt lgkmcnt(8)
	v_mfma_f32_32x32x16_bf16 v[50:65], v[230:233], v[74:77], v[50:65]
	v_max3_f32 v2, v2, v117, v118
	v_max3_f32 v2, v2, v119, v120
	v_max3_f32 v2, v2, v121, v122
	v_mfma_f32_32x32x16_bf16 v[50:65], v[234:237], v[66:69], v[50:65]
	v_max3_f32 v2, v2, v123, v124
	v_max3_f32 v2, v2, v125, v126
	v_max3_f32 v2, v2, v127, v128
	s_add_i32 s36, s35, -1
	s_cmp_lt_u32 s36, s30
	s_cselect_b32 s0, 0, s30
	s_cselect_b32 s1, s29, s34
	s_lshl_b32 s0, s0, 6
	s_sub_i32 s37, s1, s0
	s_lshl_b32 s1, s36, 6
	s_add_i32 s37, s37, s1
	s_lshl_b32 s0, s37, 6
	s_add_u32 s48, s44, s0
	s_addc_u32 s49, s45, 0
	s_lshl_b32 s0, s37, 11
	s_add_u32 s46, s42, s0
	s_addc_u32 s47, s43, 0
	global_load_dwordx4 v[174:177], v226, s[48:49]
	v_mfma_f32_32x32x16_bf16 v[50:65], v[238:241], v[70:73], v[50:65]
	v_max_f32_e32 v2, v2, v129
	s_nop 0
	s_nop 0
	global_load_dwordx4 v[8:11], v225, s[46:47]
	global_load_dwordx4 v[4:7], v225, s[46:47] offset:128
	v_mfma_f32_32x32x16_bf16 v[50:65], v[242:245], v[12:15], v[50:65]
	v_mov_b32_e32 v16, v2
	s_nop 1
	v_permlane32_swap_b32_e32 v2, v16
	v_max_f32_e32 v2, v2, v16
	v_cmp_ge_f32_e32 vcc, s28, v2
	s_cmp_eq_u64 vcc, exec
	s_cbranch_scc0 .LBB0_542
	v_mov_b32_e32 v2, 1.0

; __device__ __forceinline__ void finishSM(f32x16& p0, f32x16& p1, float alpha, float& l_reg, bf16x8& pa0, bf16x8& pa1, bf16x8& pa2, bf16x8& pa3) {
; #pragma unroll
;     for (int r = 0; r < 16; ++r) p1[r] = EXP_PROBE ? fmaf(p1[r], 0.001f, 1.f) : __builtin_amdgcn_exp2f(p1[r]);
;     float ps = 0.f;
; #pragma unroll
;     for (int r = 0; r < 16; ++r) ps += p0[r];
; #pragma unroll
;     for (int r = 0; r < 16; ++r) ps += p1[r];
;     { auto rr = __builtin_amdgcn_permlane32_swap(__float_as_uint(ps), __float_as_uint(ps), false, false);
;       ps = __uint_as_float(rr[0]) + __uint_as_float(rr[1]); }
;     l_reg = l_reg * alpha + ps;
;     ATT_PKN(p0, 0, pa0); ATT_PKN(p0, 8, pa1); ATT_PKN(p1, 0, pa2); ATT_PKN(p1, 8, pa3);
; }
; template <int DQK> __device__ __forceinline__ void qkt(f32x16& p0, f32x16& p1, const LAS char* buf, const bf16x8* qr, int r32, int hi, const f32x16& negm) {
; #pragma unroll
;     for (int d0 = 0; d0 < 4; ++d0) { const int ch = d0 * 2 + hi;
;         const bf16x8 b0 = *(const LAS bf16x8*)(buf + B_KN + swz64(r32, ch));
;         const bf16x8 b1 = *(const LAS bf16x8*)(buf + B_KN + swz64(32 + r32, ch));
;         p0 = __builtin_amdgcn_mfma_f32_32x32x16_bf16(b0, qr[d0], d0 == 0 ? negm : p0, 0, 0, 0);
;         p1 = __builtin_amdgcn_mfma_f32_32x32x16_bf16(b1, qr[d0], d0 == 0 ? negm : p1, 0, 0, 0); }
;     if constexpr (DQK == 96) {
; #pragma unroll
;         for (int d0 = 0; d0 < 2; ++d0) { const int ch = d0 * 2 + hi;
;             const bf16x8 b0 = *(const LAS bf16x8*)(buf + B_KR + swz32(r32, ch));
;             const bf16x8 b1 = *(const LAS bf16x8*)(buf + B_KR + swz32(32 + r32, ch));
;             p0 = __builtin_amdgcn_mfma_f32_32x32x16_bf16(b0, qr[4 + d0], p0, 0, 0, 0);
;             p1 = __builtin_amdgcn_mfma_f32_32x32x16_bf16(b1, qr[4 + d0], p1, 0, 0, 0); }
;     }
; }
; template <int D0> __device__ __forceinline__ void pv_one(f32x16& od, unsigned vb, bf16x8 pa0, bf16x8 pa1, bf16x8 pa2, bf16x8 pa3) {
;     const s16x4 l0 = tr_read<v_rd_off(D0, 0, 0)>(vb), h0 = tr_read<v_rd_off(D0, 0, 1)>(vb), l1 = tr_read<v_rd_off(D0, 1, 0)>(vb), h1 = tr_read<v_rd_off(D0, 1, 1)>(vb);
;     const s16x4 l2 = tr_read<v_rd_off(D0, 2, 0)>(vb), h2 = tr_read<v_rd_off(D0, 2, 1)>(vb), l3 = tr_read<v_rd_off(D0, 3, 0)>(vb), h3 = tr_read<v_rd_off(D0, 3, 1)>(vb);
;     asm volatile("s_waitcnt lgkmcnt(0)" ::: "memory"); SBAR();
.LBB0_531:
	s_waitcnt lgkmcnt(0)
	s_barrier
	v_add_u32_e32 v17, s10, v201
	v_add_u32_e32 v182, v17, v209
	ds_read_b128 v[178:181], v182
	ds_read_b128 v[182:185], v182 offset:4096
	v_add_u32_e32 v66, v17, v210
	ds_read_b128 v[170:173], v66
	ds_read_b128 v[66:69], v66 offset:4096
	v_add_u32_e32 v74, v17, v211
	ds_read_b128 v[70:73], v74
	ds_read_b128 v[74:77], v74 offset:4096
	v_add_u32_e32 v253, v17, v212
	ds_read_b128 v[78:81], v253
	v_add_u32_e32 v17, s10, v217
	v_exp_f32_e32 v114, v114
	v_exp_f32_e32 v115, v115
	v_exp_f32_e32 v116, v116
	v_exp_f32_e32 v117, v117
	v_exp_f32_e32 v118, v118
	v_exp_f32_e32 v119, v119
	v_exp_f32_e32 v120, v120
	v_exp_f32_e32 v121, v121
	s_waitcnt lgkmcnt(6)
	v_mfma_f32_32x32x16_bf16 v[130:145], v[178:181], v[166:169], v[82:97]
	ds_read_b128 v[178:181], v253 offset:4096
	v_exp_f32_e32 v122, v122
	v_exp_f32_e32 v123, v123
	v_exp_f32_e32 v124, v124
	v_cvt_pk_bf16_f32 v12, v16, v234
	s_waitcnt lgkmcnt(6)
	v_mfma_f32_32x32x16_bf16 v[98:113], v[182:185], v[166:169], v[82:97]
	v_add_u32_e32 v253, v17, v219
	ds_read_b128 v[182:185], v253 offset:8192
	v_exp_f32_e32 v125, v125
	v_exp_f32_e32 v126, v126
	v_exp_f32_e32 v127, v127
	v_cvt_pk_bf16_f32 v13, v235, v236
	s_waitcnt lgkmcnt(6)
	v_mfma_f32_32x32x16_bf16 v[130:145], v[170:173], v[162:165], v[130:145]
	ds_read_b128 v[170:173], v253 offset:10240
	v_exp_f32_e32 v128, v128
	v_exp_f32_e32 v129, v129
	v_cvt_pk_bf16_f32 v14, v237, v238
	v_cvt_pk_bf16_f32 v15, v239, v240
	v_add_f32_e32 v252, 0, v16
	v_add_f32_e32 v252, v234, v252
	s_waitcnt lgkmcnt(6)
	v_mfma_f32_32x32x16_bf16 v[98:113], v[66:69], v[162:165], v[98:113]
	v_add_u32_e32 v253, v17, v220
	ds_read_b128 v[66:69], v253 offset:8192
	v_cvt_pk_bf16_f32 v230, v241, v242
	v_cvt_pk_bf16_f32 v231, v243, v244
	v_add_f32_e32 v252, v235, v252
	v_add_f32_e32 v252, v236, v252
	v_add_f32_e32 v252, v237, v252
	v_add_f32_e32 v252, v238, v252
	s_waitcnt lgkmcnt(6)
	v_mfma_f32_32x32x16_bf16 v[130:145], v[70:73], v[158:161], v[130:145]
	ds_read_b128 v[70:73], v253 offset:10240
	v_cvt_pk_bf16_f32 v232, v245, v246
	v_cvt_pk_bf16_f32 v233, v247, v248
	v_add_f32_e32 v252, v239, v252
	v_add_f32_e32 v252, v240, v252
	v_add_f32_e32 v252, v241, v252
	v_add_f32_e32 v252, v242, v252
	s_waitcnt lgkmcnt(6)
	v_mfma_f32_32x32x16_bf16 v[98:113], v[74:77], v[158:161], v[98:113]
	v_add_f32_e32 v252, v243, v252
	v_add_f32_e32 v252, v244, v252
	v_add_f32_e32 v252, v245, v252
	v_add_f32_e32 v252, v246, v252
	v_add_f32_e32 v252, v247, v252
	v_add_f32_e32 v252, v248, v252
	s_waitcnt lgkmcnt(5)
	v_mfma_f32_32x32x16_bf16 v[130:145], v[78:81], v[154:157], v[130:145]
	v_add_u32_e32 v16, s13, v213
	ds_read_b64_tr_b16 v[234:235], v16 offset:0
	ds_read_b64_tr_b16 v[236:237], v16 offset:1024
	ds_read_b64_tr_b16 v[238:239], v16 offset:2048
	ds_read_b64_tr_b16 v[240:241], v16 offset:3072
	v_add_f32_e32 v252, v114, v252
	v_add_f32_e32 v252, v115, v252
	v_add_f32_e32 v252, v116, v252
	s_waitcnt lgkmcnt(8)
	v_mfma_f32_32x32x16_bf16 v[98:113], v[178:181], v[154:157], v[98:113]
	ds_read_b64_tr_b16 v[242:243], v16 offset:4096
	ds_read_b64_tr_b16 v[244:245], v16 offset:5120
	ds_read_b64_tr_b16 v[246:247], v16 offset:6144
	ds_read_b64_tr_b16 v[248:249], v16 offset:7168
	v_add_f32_e32 v252, v117, v252
	v_add_f32_e32 v252, v118, v252
	v_add_f32_e32 v252, v119, v252
	s_waitcnt lgkmcnt(11)
	v_mfma_f32_32x32x16_bf16 v[130:145], v[182:185], v[150:153], v[130:145]
	v_add_f32_e32 v252, v120, v252
	v_add_f32_e32 v252, v121, v252
	v_add_f32_e32 v252, v122, v252
	v_add_f32_e32 v252, v123, v252
	v_add_f32_e32 v252, v124, v252
	v_add_f32_e32 v252, v125, v252
	s_waitcnt lgkmcnt(10)
	v_mfma_f32_32x32x16_bf16 v[98:113], v[170:173], v[150:153], v[98:113]
	v_add_f32_e32 v252, v126, v252
	v_add_f32_e32 v252, v127, v252
	v_add_f32_e32 v252, v128, v252
	s_waitcnt lgkmcnt(9)
	v_mfma_f32_32x32x16_bf16 v[130:145], v[66:69], v[146:149], v[130:145]
	v_cvt_pk_bf16_f32 v114, v114, v115
	v_cvt_pk_bf16_f32 v115, v116, v117
	v_cvt_pk_bf16_f32 v116, v118, v119
	v_cvt_pk_bf16_f32 v117, v120, v121
	s_waitcnt lgkmcnt(8)
	v_mfma_f32_32x32x16_bf16 v[98:113], v[70:73], v[146:149], v[98:113]
	v_cvt_pk_bf16_f32 v118, v122, v123
	v_cvt_pk_bf16_f32 v119, v124, v125
	v_cvt_pk_bf16_f32 v120, v126, v127
	v_cvt_pk_bf16_f32 v121, v128, v129
	v_add_f32_e32 v126, v129, v252
	v_mov_b32_e32 v127, v126
	ds_read_b64_tr_b16 v[66:67], v16 offset:512
	ds_read_b64_tr_b16 v[68:69], v16 offset:1536
	ds_read_b64_tr_b16 v[70:71], v16 offset:2560
	ds_read_b64_tr_b16 v[72:73], v16 offset:3584
	ds_read_b64_tr_b16 v[74:75], v16 offset:4608
	ds_read_b64_tr_b16 v[76:77], v16 offset:5632
	ds_read_b64_tr_b16 v[78:79], v16 offset:6656
	ds_read_b64_tr_b16 v[80:81], v16 offset:7680
	v_permlane32_swap_b32_e32 v126, v127
	v_max3_f32 v250, v130, v131, v132
	v_max3_f32 v250, v250, v133, v134
	v_max3_f32 v250, v250, v135, v136
	v_max3_f32 v250, v250, v137, v138
	v_max3_f32 v250, v250, v139, v140
	v_max3_f32 v250, v250, v141, v142
	v_max3_f32 v250, v250, v143, v144
	v_max3_f32 v250, v250, v145, v98
	v_max3_f32 v250, v250, v99, v100
	s_waitcnt lgkmcnt(8)
	v_mfma_f32_32x32x16_bf16 v[50:65], v[234:237], v[12:15], v[50:65]
	v_max3_f32 v250, v250, v101, v102
	v_max3_f32 v250, v250, v103, v104
	v_max3_f32 v250, v250, v105, v106
	v_mfma_f32_32x32x16_bf16 v[50:65], v[238:241], v[230:233], v[50:65]
	v_max3_f32 v250, v250, v107, v108
	v_max3_f32 v250, v250, v109, v110
	v_max3_f32 v250, v250, v111, v112
	v_mfma_f32_32x32x16_bf16 v[50:65], v[242:245], v[114:117], v[50:65]
	v_max_f32_e32 v250, v250, v113
	s_nop 0
	s_nop 0
	s_cmp_ge_u32 s35, s31
	s_cbranch_scc1 .Lmla_b_noload
	s_cmp_lt_u32 s35, s30
	s_cselect_b32 s0, 0, s30
	s_cselect_b32 s1, s29, s34
	s_lshl_b32 s0, s0, 6
	s_sub_i32 s37, s1, s0
	s_lshl_b32 s1, s35, 6
	s_add_i32 s37, s37, s1
	s_lshl_b32 s0, s37, 6
	s_add_u32 s48, s44, s0
	s_addc_u32 s49, s45, 0
	s_lshl_b32 s0, s37, 11
	s_add_u32 s46, s42, s0
	s_addc_u32 s47, s43, 0
	global_load_dwordx4 v[170:173], v226, s[48:49]
	global_load_dwordx4 v[178:181], v225, s[46:47]
	global_load_dwordx4 v[182:185], v225, s[46:47] offset:128
.Lmla_b_ld_done:
	v_mfma_f32_32x32x16_bf16 v[50:65], v[246:249], v[118:121], v[50:65]
	v_mov_b32_e32 v251, v250
	s_nop 1
	v_permlane32_swap_b32_e32 v250, v251
	v_max_f32_e32 v250, v250, v251
	v_cmp_ge_f32_e32 vcc, s28, v250
	s_cmp_eq_u64 vcc, exec
	v_mov_b32_e32 v16, 1.0
	s_cbranch_scc0 .LBB0_543
